# speedup vs baseline: 1.0332x; 1.0113x over previous
.Lloop_k5:
	s_waitcnt vmcnt(0)
	s_barrier
	ds_read_b128 v[98:101], v94
	ds_read_b128 v[102:105], v94 offset:32768
	ds_read_b128 v[106:109], v94 offset:2048
	ds_read_b128 v[110:113], v94 offset:34816
	ds_read_b128 v[114:117], v94 offset:4096
	ds_read_b128 v[118:121], v94 offset:36864
	ds_read_b128 v[122:125], v94 offset:6144
	ds_read_b128 v[126:129], v94 offset:38912
	ds_read_b128 v[130:133], v95 offset:16384
	ds_read_b128 v[134:137], v95 offset:49152
	s_waitcnt lgkmcnt(1)
	v_mfma_f32_16x16x32_f16 v[62:65], v[98:101], v[130:133], v[62:65]
	ds_read_b128 v[138:141], v95 offset:18432
	ds_read_b128 v[142:145], v95 offset:51200
	s_waitcnt lgkmcnt(2)
	v_mfma_f32_16x16x32_f16 v[62:65], v[98:101], v[134:137], v[62:65]
	ds_read_b128 v[146:149], v95 offset:20480
	ds_read_b128 v[150:153], v95 offset:53248
	v_mfma_f32_16x16x32_f16 v[62:65], v[102:105], v[130:133], v[62:65]
	ds_read_b128 v[154:157], v95 offset:22528
	ds_read_b128 v[158:161], v95 offset:55296
	s_waitcnt lgkmcnt(5)
	v_mfma_f32_16x16x32_f16 v[58:61], v[98:101], v[138:141], v[58:61]
	ds_read_b128 v[162:165], v96
	ds_read_b128 v[166:169], v96 offset:32768
	s_waitcnt lgkmcnt(6)
	v_mfma_f32_16x16x32_f16 v[58:61], v[98:101], v[142:145], v[58:61]
	ds_read_b128 v[170:173], v96 offset:2048
	ds_read_b128 v[174:177], v96 offset:34816
	v_mfma_f32_16x16x32_f16 v[58:61], v[102:105], v[138:141], v[58:61]
	ds_read_b128 v[178:181], v96 offset:4096
	ds_read_b128 v[182:185], v96 offset:36864
	s_waitcnt lgkmcnt(9)
	v_mfma_f32_16x16x32_f16 v[54:57], v[98:101], v[146:149], v[54:57]
	ds_read_b128 v[186:189], v96 offset:6144
	ds_read_b128 v[190:193], v96 offset:38912
	s_waitcnt lgkmcnt(10)
	v_mfma_f32_16x16x32_f16 v[54:57], v[98:101], v[150:153], v[54:57]
	ds_read_b128 v[194:197], v97 offset:16384
	ds_read_b128 v[198:201], v97 offset:49152
	v_mfma_f32_16x16x32_f16 v[54:57], v[102:105], v[146:149], v[54:57]
	ds_read_b128 v[202:205], v97 offset:18432
	ds_read_b128 v[206:209], v97 offset:51200
	s_waitcnt lgkmcnt(13)
	v_mfma_f32_16x16x32_f16 v[50:53], v[98:101], v[154:157], v[50:53]
	ds_read_b128 v[210:213], v97 offset:20480
	ds_read_b128 v[214:217], v97 offset:53248
	s_waitcnt lgkmcnt(14)
	v_mfma_f32_16x16x32_f16 v[50:53], v[98:101], v[158:161], v[50:53]
	ds_read_b128 v[98:101], v97 offset:22528
	ds_read_b128 v[218:221], v97 offset:55296
	v_mfma_f32_16x16x32_f16 v[50:53], v[102:105], v[154:157], v[50:53]
	v_mfma_f32_16x16x32_f16 v[46:49], v[106:109], v[130:133], v[46:49]
	v_mfma_f32_16x16x32_f16 v[46:49], v[106:109], v[134:137], v[46:49]
	v_mfma_f32_16x16x32_f16 v[46:49], v[110:113], v[130:133], v[46:49]
	v_mfma_f32_16x16x32_f16 v[42:45], v[106:109], v[138:141], v[42:45]
	s_waitcnt lgkmcnt(0)
	s_barrier
	s_add_i32 s45, s45, -1
	s_cmp_eq_u32 s45, 0
	s_cbranch_scc1 .Llast_k5
	s_add_u32 s28, s28, 0x80
	s_addc_u32 s29, s29, 0
	s_add_u32 s30, s30, 0x80
	s_addc_u32 s31, s31, 0
	s_add_u32 s32, s32, 0x80
	s_addc_u32 s33, s33, 0
	s_add_u32 s34, s34, 0x80
	s_addc_u32 s35, s35, 0
	s_mov_b64 s[50:51], s[28:29]
	s_mov_b32 m0, s44
	v_mfma_f32_16x16x32_f16 v[42:45], v[106:109], v[142:145], v[42:45]
	global_load_lds_dwordx4 v222, s[50:51]
	v_mfma_f32_16x16x32_f16 v[42:45], v[110:113], v[138:141], v[42:45]
	v_mfma_f32_16x16x32_f16 v[38:41], v[106:109], v[146:149], v[38:41]
	v_mfma_f32_16x16x32_f16 v[38:41], v[106:109], v[150:153], v[38:41]
	v_mfma_f32_16x16x32_f16 v[38:41], v[110:113], v[146:149], v[38:41]
	s_mov_b64 s[52:53], s[32:33]
	s_add_u32 m0, s44, 0x4000
	v_mfma_f32_16x16x32_f16 v[34:37], v[106:109], v[154:157], v[34:37]
	global_load_lds_dwordx4 v223, s[52:53]
	v_mfma_f32_16x16x32_f16 v[34:37], v[106:109], v[158:161], v[34:37]
	v_mfma_f32_16x16x32_f16 v[34:37], v[110:113], v[154:157], v[34:37]
	v_mfma_f32_16x16x32_f16 v[30:33], v[114:117], v[130:133], v[30:33]
	v_mfma_f32_16x16x32_f16 v[30:33], v[114:117], v[134:137], v[30:33]
	s_mov_b64 s[50:51], s[30:31]
	s_add_u32 m0, s44, 0x8000
	v_mfma_f32_16x16x32_f16 v[30:33], v[118:121], v[130:133], v[30:33]
	global_load_lds_dwordx4 v222, s[50:51]
	v_mfma_f32_16x16x32_f16 v[26:29], v[114:117], v[138:141], v[26:29]
	v_mfma_f32_16x16x32_f16 v[26:29], v[114:117], v[142:145], v[26:29]
	v_mfma_f32_16x16x32_f16 v[26:29], v[118:121], v[138:141], v[26:29]
	v_mfma_f32_16x16x32_f16 v[22:25], v[114:117], v[146:149], v[22:25]
	s_mov_b64 s[52:53], s[34:35]
	s_add_u32 m0, s44, 0xc000
	v_mfma_f32_16x16x32_f16 v[22:25], v[114:117], v[150:153], v[22:25]
	global_load_lds_dwordx4 v223, s[52:53]
	v_mfma_f32_16x16x32_f16 v[22:25], v[118:121], v[146:149], v[22:25]
	v_mfma_f32_16x16x32_f16 v[18:21], v[114:117], v[154:157], v[18:21]
	v_mfma_f32_16x16x32_f16 v[18:21], v[114:117], v[158:161], v[18:21]
	v_mfma_f32_16x16x32_f16 v[18:21], v[118:121], v[154:157], v[18:21]
	s_add_u32 s50, s28, s38
	s_addc_u32 s51, s29, 0
	s_add_u32 m0, s44, 0x1000
	v_mfma_f32_16x16x32_f16 v[14:17], v[122:125], v[130:133], v[14:17]
	global_load_lds_dwordx4 v222, s[50:51]
	v_mfma_f32_16x16x32_f16 v[14:17], v[122:125], v[134:137], v[14:17]
	v_mfma_f32_16x16x32_f16 v[14:17], v[126:129], v[130:133], v[14:17]
	v_mfma_f32_16x16x32_f16 v[10:13], v[122:125], v[138:141], v[10:13]
	v_mfma_f32_16x16x32_f16 v[10:13], v[122:125], v[142:145], v[10:13]
	s_add_u32 s52, s32, s41
	s_addc_u32 s53, s33, 0
	s_add_u32 m0, s44, 0x5000
	v_mfma_f32_16x16x32_f16 v[10:13], v[126:129], v[138:141], v[10:13]
	global_load_lds_dwordx4 v223, s[52:53]
	v_mfma_f32_16x16x32_f16 v[6:9], v[122:125], v[146:149], v[6:9]
	v_mfma_f32_16x16x32_f16 v[6:9], v[122:125], v[150:153], v[6:9]
	v_mfma_f32_16x16x32_f16 v[6:9], v[126:129], v[146:149], v[6:9]
	v_mfma_f32_16x16x32_f16 v[2:5], v[122:125], v[154:157], v[2:5]
	s_add_u32 s50, s30, s38
	s_addc_u32 s51, s31, 0
	s_add_u32 m0, s44, 0x9000
	v_mfma_f32_16x16x32_f16 v[2:5], v[122:125], v[158:161], v[2:5]
	global_load_lds_dwordx4 v222, s[50:51]
	v_mfma_f32_16x16x32_f16 v[2:5], v[126:129], v[154:157], v[2:5]
	s_waitcnt lgkmcnt(7)
	v_mfma_f32_16x16x32_f16 v[62:65], v[162:165], v[194:197], v[62:65]
	s_waitcnt lgkmcnt(6)
	v_mfma_f32_16x16x32_f16 v[62:65], v[162:165], v[198:201], v[62:65]
	v_mfma_f32_16x16x32_f16 v[62:65], v[166:169], v[194:197], v[62:65]
	s_add_u32 s52, s34, s41
	s_addc_u32 s53, s35, 0
	s_add_u32 m0, s44, 0xd000
	s_waitcnt lgkmcnt(5)
	v_mfma_f32_16x16x32_f16 v[58:61], v[162:165], v[202:205], v[58:61]
	global_load_lds_dwordx4 v223, s[52:53]
	s_waitcnt lgkmcnt(4)
	v_mfma_f32_16x16x32_f16 v[58:61], v[162:165], v[206:209], v[58:61]
	v_mfma_f32_16x16x32_f16 v[58:61], v[166:169], v[202:205], v[58:61]
	s_waitcnt lgkmcnt(3)
	v_mfma_f32_16x16x32_f16 v[54:57], v[162:165], v[210:213], v[54:57]
	s_waitcnt lgkmcnt(2)
	v_mfma_f32_16x16x32_f16 v[54:57], v[162:165], v[214:217], v[54:57]
	s_add_u32 s50, s28, s39
	s_addc_u32 s51, s29, 0
	s_add_u32 m0, s44, 0x2000
	v_mfma_f32_16x16x32_f16 v[54:57], v[166:169], v[210:213], v[54:57]
	global_load_lds_dwordx4 v222, s[50:51]
	s_waitcnt lgkmcnt(1)
	v_mfma_f32_16x16x32_f16 v[50:53], v[162:165], v[98:101], v[50:53]
	s_waitcnt lgkmcnt(0)
	v_mfma_f32_16x16x32_f16 v[50:53], v[162:165], v[218:221], v[50:53]
	v_mfma_f32_16x16x32_f16 v[50:53], v[166:169], v[98:101], v[50:53]
	v_mfma_f32_16x16x32_f16 v[46:49], v[170:173], v[194:197], v[46:49]
	s_add_u32 s52, s32, s42
	s_addc_u32 s53, s33, 0
	s_add_u32 m0, s44, 0x6000
	v_mfma_f32_16x16x32_f16 v[46:49], v[170:173], v[198:201], v[46:49]
	global_load_lds_dwordx4 v223, s[52:53]
	v_mfma_f32_16x16x32_f16 v[46:49], v[174:177], v[194:197], v[46:49]
	v_mfma_f32_16x16x32_f16 v[42:45], v[170:173], v[202:205], v[42:45]
	v_mfma_f32_16x16x32_f16 v[42:45], v[170:173], v[206:209], v[42:45]
	v_mfma_f32_16x16x32_f16 v[42:45], v[174:177], v[202:205], v[42:45]
	s_add_u32 s50, s30, s39
	s_addc_u32 s51, s31, 0
	s_add_u32 m0, s44, 0xa000
	v_mfma_f32_16x16x32_f16 v[38:41], v[170:173], v[210:213], v[38:41]
	global_load_lds_dwordx4 v222, s[50:51]
	v_mfma_f32_16x16x32_f16 v[38:41], v[170:173], v[214:217], v[38:41]
	v_mfma_f32_16x16x32_f16 v[38:41], v[174:177], v[210:213], v[38:41]
	v_mfma_f32_16x16x32_f16 v[34:37], v[170:173], v[98:101], v[34:37]
	v_mfma_f32_16x16x32_f16 v[34:37], v[170:173], v[218:221], v[34:37]
	s_add_u32 s52, s34, s42
	s_addc_u32 s53, s35, 0
	s_add_u32 m0, s44, 0xe000
	v_mfma_f32_16x16x32_f16 v[34:37], v[174:177], v[98:101], v[34:37]
	global_load_lds_dwordx4 v223, s[52:53]
	v_mfma_f32_16x16x32_f16 v[30:33], v[178:181], v[194:197], v[30:33]
	v_mfma_f32_16x16x32_f16 v[30:33], v[178:181], v[198:201], v[30:33]
	v_mfma_f32_16x16x32_f16 v[30:33], v[182:185], v[194:197], v[30:33]
	v_mfma_f32_16x16x32_f16 v[26:29], v[178:181], v[202:205], v[26:29]
	s_add_u32 s50, s28, s40
	s_addc_u32 s51, s29, 0
	s_add_u32 m0, s44, 0x3000
	v_mfma_f32_16x16x32_f16 v[26:29], v[178:181], v[206:209], v[26:29]
	global_load_lds_dwordx4 v222, s[50:51]
	v_mfma_f32_16x16x32_f16 v[26:29], v[182:185], v[202:205], v[26:29]
	v_mfma_f32_16x16x32_f16 v[22:25], v[178:181], v[210:213], v[22:25]
	v_mfma_f32_16x16x32_f16 v[22:25], v[178:181], v[214:217], v[22:25]
	v_mfma_f32_16x16x32_f16 v[22:25], v[182:185], v[210:213], v[22:25]
	s_add_u32 s52, s32, s43
	s_addc_u32 s53, s33, 0
	s_add_u32 m0, s44, 0x7000
	v_mfma_f32_16x16x32_f16 v[18:21], v[178:181], v[98:101], v[18:21]
	global_load_lds_dwordx4 v223, s[52:53]
	v_mfma_f32_16x16x32_f16 v[18:21], v[178:181], v[218:221], v[18:21]
	v_mfma_f32_16x16x32_f16 v[18:21], v[182:185], v[98:101], v[18:21]
	v_mfma_f32_16x16x32_f16 v[14:17], v[186:189], v[194:197], v[14:17]
	v_mfma_f32_16x16x32_f16 v[14:17], v[186:189], v[198:201], v[14:17]
	s_add_u32 s50, s30, s40
	s_addc_u32 s51, s31, 0
	s_add_u32 m0, s44, 0xb000
	v_mfma_f32_16x16x32_f16 v[14:17], v[190:193], v[194:197], v[14:17]
	global_load_lds_dwordx4 v222, s[50:51]
	v_mfma_f32_16x16x32_f16 v[10:13], v[186:189], v[202:205], v[10:13]
	v_mfma_f32_16x16x32_f16 v[10:13], v[186:189], v[206:209], v[10:13]
	v_mfma_f32_16x16x32_f16 v[10:13], v[190:193], v[202:205], v[10:13]
	v_mfma_f32_16x16x32_f16 v[6:9], v[186:189], v[210:213], v[6:9]
	s_add_u32 s52, s34, s43
	s_addc_u32 s53, s35, 0
	s_add_u32 m0, s44, 0xf000
	v_mfma_f32_16x16x32_f16 v[6:9], v[186:189], v[214:217], v[6:9]
	global_load_lds_dwordx4 v223, s[52:53]
	v_mfma_f32_16x16x32_f16 v[6:9], v[190:193], v[210:213], v[6:9]
	v_mfma_f32_16x16x32_f16 v[2:5], v[186:189], v[98:101], v[2:5]
	v_mfma_f32_16x16x32_f16 v[2:5], v[186:189], v[218:221], v[2:5]
	v_mfma_f32_16x16x32_f16 v[2:5], v[190:193], v[98:101], v[2:5]
	s_branch .Lloop_k5
.Llast_k5:
	v_mfma_f32_16x16x32_f16 v[42:45], v[106:109], v[142:145], v[42:45]
	v_mfma_f32_16x16x32_f16 v[42:45], v[110:113], v[138:141], v[42:45]
	v_mfma_f32_16x16x32_f16 v[38:41], v[106:109], v[146:149], v[38:41]
	v_mfma_f32_16x16x32_f16 v[38:41], v[106:109], v[150:153], v[38:41]
	v_mfma_f32_16x16x32_f16 v[38:41], v[110:113], v[146:149], v[38:41]
	v_mfma_f32_16x16x32_f16 v[34:37], v[106:109], v[154:157], v[34:37]
	v_mfma_f32_16x16x32_f16 v[34:37], v[106:109], v[158:161], v[34:37]
	v_mfma_f32_16x16x32_f16 v[34:37], v[110:113], v[154:157], v[34:37]
	v_mfma_f32_16x16x32_f16 v[30:33], v[114:117], v[130:133], v[30:33]
	v_mfma_f32_16x16x32_f16 v[30:33], v[114:117], v[134:137], v[30:33]
	v_mfma_f32_16x16x32_f16 v[30:33], v[118:121], v[130:133], v[30:33]
	v_mfma_f32_16x16x32_f16 v[26:29], v[114:117], v[138:141], v[26:29]
	v_mfma_f32_16x16x32_f16 v[26:29], v[114:117], v[142:145], v[26:29]
	v_mfma_f32_16x16x32_f16 v[26:29], v[118:121], v[138:141], v[26:29]
	v_mfma_f32_16x16x32_f16 v[22:25], v[114:117], v[146:149], v[22:25]
	v_mfma_f32_16x16x32_f16 v[22:25], v[114:117], v[150:153], v[22:25]
	v_mfma_f32_16x16x32_f16 v[22:25], v[118:121], v[146:149], v[22:25]
	v_mfma_f32_16x16x32_f16 v[18:21], v[114:117], v[154:157], v[18:21]
	v_mfma_f32_16x16x32_f16 v[18:21], v[114:117], v[158:161], v[18:21]
	v_mfma_f32_16x16x32_f16 v[18:21], v[118:121], v[154:157], v[18:21]
	v_mfma_f32_16x16x32_f16 v[14:17], v[122:125], v[130:133], v[14:17]
	v_mfma_f32_16x16x32_f16 v[14:17], v[122:125], v[134:137], v[14:17]
	v_mfma_f32_16x16x32_f16 v[14:17], v[126:129], v[130:133], v[14:17]
	v_mfma_f32_16x16x32_f16 v[10:13], v[122:125], v[138:141], v[10:13]
	v_mfma_f32_16x16x32_f16 v[10:13], v[122:125], v[142:145], v[10:13]
	v_mfma_f32_16x16x32_f16 v[10:13], v[126:129], v[138:141], v[10:13]
	v_mfma_f32_16x16x32_f16 v[6:9], v[122:125], v[146:149], v[6:9]
	v_mfma_f32_16x16x32_f16 v[6:9], v[122:125], v[150:153], v[6:9]
	v_mfma_f32_16x16x32_f16 v[6:9], v[126:129], v[146:149], v[6:9]
	v_mfma_f32_16x16x32_f16 v[2:5], v[122:125], v[154:157], v[2:5]
	v_mfma_f32_16x16x32_f16 v[2:5], v[122:125], v[158:161], v[2:5]
	v_mfma_f32_16x16x32_f16 v[2:5], v[126:129], v[154:157], v[2:5]
	s_waitcnt lgkmcnt(7)
	v_mfma_f32_16x16x32_f16 v[62:65], v[162:165], v[194:197], v[62:65]
	s_waitcnt lgkmcnt(6)
	v_mfma_f32_16x16x32_f16 v[62:65], v[162:165], v[198:201], v[62:65]
	v_mfma_f32_16x16x32_f16 v[62:65], v[166:169], v[194:197], v[62:65]
	s_waitcnt lgkmcnt(5)
	v_mfma_f32_16x16x32_f16 v[58:61], v[162:165], v[202:205], v[58:61]
	s_waitcnt lgkmcnt(4)
	v_mfma_f32_16x16x32_f16 v[58:61], v[162:165], v[206:209], v[58:61]
	v_mfma_f32_16x16x32_f16 v[58:61], v[166:169], v[202:205], v[58:61]
	s_waitcnt lgkmcnt(3)
	v_mfma_f32_16x16x32_f16 v[54:57], v[162:165], v[210:213], v[54:57]
	s_waitcnt lgkmcnt(2)
	v_mfma_f32_16x16x32_f16 v[54:57], v[162:165], v[214:217], v[54:57]
	v_mfma_f32_16x16x32_f16 v[54:57], v[166:169], v[210:213], v[54:57]
	s_waitcnt lgkmcnt(1)
	v_mfma_f32_16x16x32_f16 v[50:53], v[162:165], v[98:101], v[50:53]
	s_waitcnt lgkmcnt(0)
	v_mfma_f32_16x16x32_f16 v[50:53], v[162:165], v[218:221], v[50:53]
	v_mfma_f32_16x16x32_f16 v[50:53], v[166:169], v[98:101], v[50:53]
	v_mfma_f32_16x16x32_f16 v[46:49], v[170:173], v[194:197], v[46:49]
	v_mfma_f32_16x16x32_f16 v[46:49], v[170:173], v[198:201], v[46:49]
	v_mfma_f32_16x16x32_f16 v[46:49], v[174:177], v[194:197], v[46:49]
	v_mfma_f32_16x16x32_f16 v[42:45], v[170:173], v[202:205], v[42:45]
	v_mfma_f32_16x16x32_f16 v[42:45], v[170:173], v[206:209], v[42:45]
	v_mfma_f32_16x16x32_f16 v[42:45], v[174:177], v[202:205], v[42:45]
	v_mfma_f32_16x16x32_f16 v[38:41], v[170:173], v[210:213], v[38:41]
	v_mfma_f32_16x16x32_f16 v[38:41], v[170:173], v[214:217], v[38:41]
	v_mfma_f32_16x16x32_f16 v[38:41], v[174:177], v[210:213], v[38:41]
	v_mfma_f32_16x16x32_f16 v[34:37], v[170:173], v[98:101], v[34:37]
	v_mfma_f32_16x16x32_f16 v[34:37], v[170:173], v[218:221], v[34:37]
	v_mfma_f32_16x16x32_f16 v[34:37], v[174:177], v[98:101], v[34:37]
	v_mfma_f32_16x16x32_f16 v[30:33], v[178:181], v[194:197], v[30:33]
	v_mfma_f32_16x16x32_f16 v[30:33], v[178:181], v[198:201], v[30:33]
	v_mfma_f32_16x16x32_f16 v[30:33], v[182:185], v[194:197], v[30:33]
	v_mfma_f32_16x16x32_f16 v[26:29], v[178:181], v[202:205], v[26:29]
	v_mfma_f32_16x16x32_f16 v[26:29], v[178:181], v[206:209], v[26:29]
	v_mfma_f32_16x16x32_f16 v[26:29], v[182:185], v[202:205], v[26:29]
	v_mfma_f32_16x16x32_f16 v[22:25], v[178:181], v[210:213], v[22:25]
	v_mfma_f32_16x16x32_f16 v[22:25], v[178:181], v[214:217], v[22:25]
	v_mfma_f32_16x16x32_f16 v[22:25], v[182:185], v[210:213], v[22:25]
	v_mfma_f32_16x16x32_f16 v[18:21], v[178:181], v[98:101], v[18:21]
	v_mfma_f32_16x16x32_f16 v[18:21], v[178:181], v[218:221], v[18:21]
	v_mfma_f32_16x16x32_f16 v[18:21], v[182:185], v[98:101], v[18:21]
	v_mfma_f32_16x16x32_f16 v[14:17], v[186:189], v[194:197], v[14:17]
	v_mfma_f32_16x16x32_f16 v[14:17], v[186:189], v[198:201], v[14:17]
	v_mfma_f32_16x16x32_f16 v[14:17], v[190:193], v[194:197], v[14:17]
	v_mfma_f32_16x16x32_f16 v[10:13], v[186:189], v[202:205], v[10:13]
	v_mfma_f32_16x16x32_f16 v[10:13], v[186:189], v[206:209], v[10:13]
	v_mfma_f32_16x16x32_f16 v[10:13], v[190:193], v[202:205], v[10:13]
	v_mfma_f32_16x16x32_f16 v[6:9], v[186:189], v[210:213], v[6:9]
	v_mfma_f32_16x16x32_f16 v[6:9], v[186:189], v[214:217], v[6:9]
	v_mfma_f32_16x16x32_f16 v[6:9], v[190:193], v[210:213], v[6:9]
	v_mfma_f32_16x16x32_f16 v[2:5], v[186:189], v[98:101], v[2:5]
	v_mfma_f32_16x16x32_f16 v[2:5], v[186:189], v[218:221], v[2:5]
	v_mfma_f32_16x16x32_f16 v[2:5], v[190:193], v[98:101], v[2:5]

.Lloop_k12:
	s_waitcnt vmcnt(0)
	s_barrier
	ds_read_b128 v[98:101], v93
	ds_read_b128 v[102:105], v93 offset:32768
	ds_read_b128 v[106:109], v93 offset:2048
	ds_read_b128 v[110:113], v93 offset:34816
	ds_read_b128 v[114:117], v93 offset:4096
	ds_read_b128 v[118:121], v93 offset:36864
	ds_read_b128 v[122:125], v93 offset:6144
	ds_read_b128 v[126:129], v93 offset:38912
	ds_read_b128 v[130:133], v94 offset:16384
	ds_read_b128 v[134:137], v94 offset:49152
	s_waitcnt lgkmcnt(1)
	v_mfma_f32_16x16x32_f16 v[62:65], v[98:101], v[130:133], v[62:65]
	ds_read_b128 v[138:141], v94 offset:18432
	ds_read_b128 v[142:145], v94 offset:51200
	s_waitcnt lgkmcnt(2)
	v_mfma_f32_16x16x32_f16 v[62:65], v[98:101], v[134:137], v[62:65]
	ds_read_b128 v[146:149], v94 offset:20480
	ds_read_b128 v[150:153], v94 offset:53248
	v_mfma_f32_16x16x32_f16 v[62:65], v[102:105], v[130:133], v[62:65]
	ds_read_b128 v[154:157], v94 offset:22528
	ds_read_b128 v[158:161], v94 offset:55296
	s_waitcnt lgkmcnt(5)
	v_mfma_f32_16x16x32_f16 v[58:61], v[98:101], v[138:141], v[58:61]
	ds_read_b128 v[162:165], v95
	ds_read_b128 v[166:169], v95 offset:32768
	s_waitcnt lgkmcnt(6)
	v_mfma_f32_16x16x32_f16 v[58:61], v[98:101], v[142:145], v[58:61]
	ds_read_b128 v[170:173], v95 offset:2048
	ds_read_b128 v[174:177], v95 offset:34816
	v_mfma_f32_16x16x32_f16 v[58:61], v[102:105], v[138:141], v[58:61]
	ds_read_b128 v[178:181], v95 offset:4096
	ds_read_b128 v[182:185], v95 offset:36864
	s_waitcnt lgkmcnt(9)
	v_mfma_f32_16x16x32_f16 v[54:57], v[98:101], v[146:149], v[54:57]
	ds_read_b128 v[186:189], v95 offset:6144
	ds_read_b128 v[190:193], v95 offset:38912
	s_waitcnt lgkmcnt(10)
	v_mfma_f32_16x16x32_f16 v[54:57], v[98:101], v[150:153], v[54:57]
	ds_read_b128 v[194:197], v96 offset:16384
	ds_read_b128 v[198:201], v96 offset:49152
	v_mfma_f32_16x16x32_f16 v[54:57], v[102:105], v[146:149], v[54:57]
	ds_read_b128 v[202:205], v96 offset:18432
	ds_read_b128 v[206:209], v96 offset:51200
	s_waitcnt lgkmcnt(13)
	v_mfma_f32_16x16x32_f16 v[50:53], v[98:101], v[154:157], v[50:53]
	ds_read_b128 v[210:213], v96 offset:20480
	ds_read_b128 v[214:217], v96 offset:53248
	s_waitcnt lgkmcnt(14)
	v_mfma_f32_16x16x32_f16 v[50:53], v[98:101], v[158:161], v[50:53]
	ds_read_b128 v[98:101], v96 offset:22528
	ds_read_b128 v[218:221], v96 offset:55296
	v_mfma_f32_16x16x32_f16 v[50:53], v[102:105], v[154:157], v[50:53]
	v_mfma_f32_16x16x32_f16 v[46:49], v[106:109], v[130:133], v[46:49]
	v_mfma_f32_16x16x32_f16 v[46:49], v[106:109], v[134:137], v[46:49]
	v_mfma_f32_16x16x32_f16 v[46:49], v[110:113], v[130:133], v[46:49]
	v_mfma_f32_16x16x32_f16 v[42:45], v[106:109], v[138:141], v[42:45]
	s_waitcnt lgkmcnt(0)
	s_barrier
	s_add_i32 s45, s45, -1
	s_cmp_eq_u32 s45, 0
	s_cbranch_scc1 .Llast_k12
	s_add_u32 s28, s28, 0x80
	s_addc_u32 s29, s29, 0
	s_add_u32 s30, s30, 0x80
	s_addc_u32 s31, s31, 0
	s_add_u32 s32, s32, 0x80
	s_addc_u32 s33, s33, 0
	s_add_u32 s34, s34, 0x80
	s_addc_u32 s35, s35, 0
	s_mov_b64 s[50:51], s[28:29]
	s_mov_b32 m0, s44
	v_mfma_f32_16x16x32_f16 v[42:45], v[106:109], v[142:145], v[42:45]
	global_load_lds_dwordx4 v222, s[50:51]
	v_mfma_f32_16x16x32_f16 v[42:45], v[110:113], v[138:141], v[42:45]
	v_mfma_f32_16x16x32_f16 v[38:41], v[106:109], v[146:149], v[38:41]
	v_mfma_f32_16x16x32_f16 v[38:41], v[106:109], v[150:153], v[38:41]
	v_mfma_f32_16x16x32_f16 v[38:41], v[110:113], v[146:149], v[38:41]
	s_mov_b64 s[52:53], s[32:33]
	s_add_u32 m0, s44, 0x4000
	v_mfma_f32_16x16x32_f16 v[34:37], v[106:109], v[154:157], v[34:37]
	global_load_lds_dwordx4 v223, s[52:53]
	v_mfma_f32_16x16x32_f16 v[34:37], v[106:109], v[158:161], v[34:37]
	v_mfma_f32_16x16x32_f16 v[34:37], v[110:113], v[154:157], v[34:37]
	v_mfma_f32_16x16x32_f16 v[30:33], v[114:117], v[130:133], v[30:33]
	v_mfma_f32_16x16x32_f16 v[30:33], v[114:117], v[134:137], v[30:33]
	s_mov_b64 s[50:51], s[30:31]
	s_add_u32 m0, s44, 0x8000
	v_mfma_f32_16x16x32_f16 v[30:33], v[118:121], v[130:133], v[30:33]
	global_load_lds_dwordx4 v222, s[50:51]
	v_mfma_f32_16x16x32_f16 v[26:29], v[114:117], v[138:141], v[26:29]
	v_mfma_f32_16x16x32_f16 v[26:29], v[114:117], v[142:145], v[26:29]
	v_mfma_f32_16x16x32_f16 v[26:29], v[118:121], v[138:141], v[26:29]
	v_mfma_f32_16x16x32_f16 v[22:25], v[114:117], v[146:149], v[22:25]
	s_mov_b64 s[52:53], s[34:35]
	s_add_u32 m0, s44, 0xc000
	v_mfma_f32_16x16x32_f16 v[22:25], v[114:117], v[150:153], v[22:25]
	global_load_lds_dwordx4 v223, s[52:53]
	v_mfma_f32_16x16x32_f16 v[22:25], v[118:121], v[146:149], v[22:25]
	v_mfma_f32_16x16x32_f16 v[18:21], v[114:117], v[154:157], v[18:21]
	v_mfma_f32_16x16x32_f16 v[18:21], v[114:117], v[158:161], v[18:21]
	v_mfma_f32_16x16x32_f16 v[18:21], v[118:121], v[154:157], v[18:21]
	s_add_u32 s50, s28, s38
	s_addc_u32 s51, s29, 0
	s_add_u32 m0, s44, 0x1000
	v_mfma_f32_16x16x32_f16 v[14:17], v[122:125], v[130:133], v[14:17]
	global_load_lds_dwordx4 v222, s[50:51]
	v_mfma_f32_16x16x32_f16 v[14:17], v[122:125], v[134:137], v[14:17]
	v_mfma_f32_16x16x32_f16 v[14:17], v[126:129], v[130:133], v[14:17]
	v_mfma_f32_16x16x32_f16 v[10:13], v[122:125], v[138:141], v[10:13]
	v_mfma_f32_16x16x32_f16 v[10:13], v[122:125], v[142:145], v[10:13]
	s_add_u32 s52, s32, s41
	s_addc_u32 s53, s33, 0
	s_add_u32 m0, s44, 0x5000
	v_mfma_f32_16x16x32_f16 v[10:13], v[126:129], v[138:141], v[10:13]
	global_load_lds_dwordx4 v223, s[52:53]
	v_mfma_f32_16x16x32_f16 v[6:9], v[122:125], v[146:149], v[6:9]
	v_mfma_f32_16x16x32_f16 v[6:9], v[122:125], v[150:153], v[6:9]
	v_mfma_f32_16x16x32_f16 v[6:9], v[126:129], v[146:149], v[6:9]
	v_mfma_f32_16x16x32_f16 v[2:5], v[122:125], v[154:157], v[2:5]
	s_add_u32 s50, s30, s38
	s_addc_u32 s51, s31, 0
	s_add_u32 m0, s44, 0x9000
	v_mfma_f32_16x16x32_f16 v[2:5], v[122:125], v[158:161], v[2:5]
	global_load_lds_dwordx4 v222, s[50:51]
	v_mfma_f32_16x16x32_f16 v[2:5], v[126:129], v[154:157], v[2:5]
	s_waitcnt lgkmcnt(7)
	v_mfma_f32_16x16x32_f16 v[62:65], v[162:165], v[194:197], v[62:65]
	s_waitcnt lgkmcnt(6)
	v_mfma_f32_16x16x32_f16 v[62:65], v[162:165], v[198:201], v[62:65]
	v_mfma_f32_16x16x32_f16 v[62:65], v[166:169], v[194:197], v[62:65]
	s_add_u32 s52, s34, s41
	s_addc_u32 s53, s35, 0
	s_add_u32 m0, s44, 0xd000
	s_waitcnt lgkmcnt(5)
	v_mfma_f32_16x16x32_f16 v[58:61], v[162:165], v[202:205], v[58:61]
	global_load_lds_dwordx4 v223, s[52:53]
	s_waitcnt lgkmcnt(4)
	v_mfma_f32_16x16x32_f16 v[58:61], v[162:165], v[206:209], v[58:61]
	v_mfma_f32_16x16x32_f16 v[58:61], v[166:169], v[202:205], v[58:61]
	s_waitcnt lgkmcnt(3)
	v_mfma_f32_16x16x32_f16 v[54:57], v[162:165], v[210:213], v[54:57]
	s_waitcnt lgkmcnt(2)
	v_mfma_f32_16x16x32_f16 v[54:57], v[162:165], v[214:217], v[54:57]
	s_add_u32 s50, s28, s39
	s_addc_u32 s51, s29, 0
	s_add_u32 m0, s44, 0x2000
	v_mfma_f32_16x16x32_f16 v[54:57], v[166:169], v[210:213], v[54:57]
	global_load_lds_dwordx4 v222, s[50:51]
	s_waitcnt lgkmcnt(1)
	v_mfma_f32_16x16x32_f16 v[50:53], v[162:165], v[98:101], v[50:53]
	s_waitcnt lgkmcnt(0)
	v_mfma_f32_16x16x32_f16 v[50:53], v[162:165], v[218:221], v[50:53]
	v_mfma_f32_16x16x32_f16 v[50:53], v[166:169], v[98:101], v[50:53]
	v_mfma_f32_16x16x32_f16 v[46:49], v[170:173], v[194:197], v[46:49]
	s_add_u32 s52, s32, s42
	s_addc_u32 s53, s33, 0
	s_add_u32 m0, s44, 0x6000
	v_mfma_f32_16x16x32_f16 v[46:49], v[170:173], v[198:201], v[46:49]
	global_load_lds_dwordx4 v223, s[52:53]
	v_mfma_f32_16x16x32_f16 v[46:49], v[174:177], v[194:197], v[46:49]
	v_mfma_f32_16x16x32_f16 v[42:45], v[170:173], v[202:205], v[42:45]
	v_mfma_f32_16x16x32_f16 v[42:45], v[170:173], v[206:209], v[42:45]
	v_mfma_f32_16x16x32_f16 v[42:45], v[174:177], v[202:205], v[42:45]
	s_add_u32 s50, s30, s39
	s_addc_u32 s51, s31, 0
	s_add_u32 m0, s44, 0xa000
	v_mfma_f32_16x16x32_f16 v[38:41], v[170:173], v[210:213], v[38:41]
	global_load_lds_dwordx4 v222, s[50:51]
	v_mfma_f32_16x16x32_f16 v[38:41], v[170:173], v[214:217], v[38:41]
	v_mfma_f32_16x16x32_f16 v[38:41], v[174:177], v[210:213], v[38:41]
	v_mfma_f32_16x16x32_f16 v[34:37], v[170:173], v[98:101], v[34:37]
	v_mfma_f32_16x16x32_f16 v[34:37], v[170:173], v[218:221], v[34:37]
	s_add_u32 s52, s34, s42
	s_addc_u32 s53, s35, 0
	s_add_u32 m0, s44, 0xe000
	v_mfma_f32_16x16x32_f16 v[34:37], v[174:177], v[98:101], v[34:37]
	global_load_lds_dwordx4 v223, s[52:53]
	v_mfma_f32_16x16x32_f16 v[30:33], v[178:181], v[194:197], v[30:33]
	v_mfma_f32_16x16x32_f16 v[30:33], v[178:181], v[198:201], v[30:33]
	v_mfma_f32_16x16x32_f16 v[30:33], v[182:185], v[194:197], v[30:33]
	v_mfma_f32_16x16x32_f16 v[26:29], v[178:181], v[202:205], v[26:29]
	s_add_u32 s50, s28, s40
	s_addc_u32 s51, s29, 0
	s_add_u32 m0, s44, 0x3000
	v_mfma_f32_16x16x32_f16 v[26:29], v[178:181], v[206:209], v[26:29]
	global_load_lds_dwordx4 v222, s[50:51]
	v_mfma_f32_16x16x32_f16 v[26:29], v[182:185], v[202:205], v[26:29]
	v_mfma_f32_16x16x32_f16 v[22:25], v[178:181], v[210:213], v[22:25]
	v_mfma_f32_16x16x32_f16 v[22:25], v[178:181], v[214:217], v[22:25]
	v_mfma_f32_16x16x32_f16 v[22:25], v[182:185], v[210:213], v[22:25]
	s_add_u32 s52, s32, s43
	s_addc_u32 s53, s33, 0
	s_add_u32 m0, s44, 0x7000
	v_mfma_f32_16x16x32_f16 v[18:21], v[178:181], v[98:101], v[18:21]
	global_load_lds_dwordx4 v223, s[52:53]
	v_mfma_f32_16x16x32_f16 v[18:21], v[178:181], v[218:221], v[18:21]
	v_mfma_f32_16x16x32_f16 v[18:21], v[182:185], v[98:101], v[18:21]
	v_mfma_f32_16x16x32_f16 v[14:17], v[186:189], v[194:197], v[14:17]
	v_mfma_f32_16x16x32_f16 v[14:17], v[186:189], v[198:201], v[14:17]
	s_add_u32 s50, s30, s40
	s_addc_u32 s51, s31, 0
	s_add_u32 m0, s44, 0xb000
	v_mfma_f32_16x16x32_f16 v[14:17], v[190:193], v[194:197], v[14:17]
	global_load_lds_dwordx4 v222, s[50:51]
	v_mfma_f32_16x16x32_f16 v[10:13], v[186:189], v[202:205], v[10:13]
	v_mfma_f32_16x16x32_f16 v[10:13], v[186:189], v[206:209], v[10:13]
	v_mfma_f32_16x16x32_f16 v[10:13], v[190:193], v[202:205], v[10:13]
	v_mfma_f32_16x16x32_f16 v[6:9], v[186:189], v[210:213], v[6:9]
	s_add_u32 s52, s34, s43
	s_addc_u32 s53, s35, 0
	s_add_u32 m0, s44, 0xf000
	v_mfma_f32_16x16x32_f16 v[6:9], v[186:189], v[214:217], v[6:9]
	global_load_lds_dwordx4 v223, s[52:53]
	v_mfma_f32_16x16x32_f16 v[6:9], v[190:193], v[210:213], v[6:9]
	v_mfma_f32_16x16x32_f16 v[2:5], v[186:189], v[98:101], v[2:5]
	v_mfma_f32_16x16x32_f16 v[2:5], v[186:189], v[218:221], v[2:5]
	v_mfma_f32_16x16x32_f16 v[2:5], v[190:193], v[98:101], v[2:5]
	s_branch .Lloop_k12
